# v42 + RG-LRU passes: the half-block s_sleep stagger of the backward waves removed
# baseline (speedup 1.0000x reference)
; #define LAS __attribute__((address_space(3)))
; __device__ __forceinline__ int crow(int r, int hh) { return (r & 3) + 8 * (r >> 2) + 4 * hh; }
; template <bool FINAL, int z> __device__ __forceinline__ void rglru_blocks(LAS unsigned char* XCB, LAS float* XCF, LAS float* HS, const bf16x8 (&wa)[8], const bf16x8 (&wx)[8],
;         float ba, float bxx, float sp8, int r, int hh, int chl, float& st, float& CA, float& CB) {
;     ...
;         for (int bi = 0; bi < 2; ++bi) { const int tb = z ? 1 - bi : bi;
;             if (z == 1 && bi == 0) __builtin_amdgcn_s_sleep(8);
;             f32x16 ya, yx;
; #pragma unroll
;             for (int i = 0; i < 16; ++i) { ya[i] = ba; yx[i] = bxx; }
; #pragma unroll
;             for (int s = 0; s < 8; ++s) { const bf16x8 af = *(const LAS bf16x8*)(XCB + (32 * tb + r) * 272 + (16 * s + 8 * hh) * 2);
;                 ya = __builtin_amdgcn_mfma_f32_32x32x16_bf16(af, wa[s], ya, 0, 0, 0); yx = __builtin_amdgcn_mfma_f32_32x32x16_bf16(af, wx[s], yx, 0, 0, 0); }
;             float av[16], bv[16];
; #pragma unroll
;             for (int i = 0; i < 16; i += 2) {
;                 typedef float f2 __attribute__((ext_vector_type(2)));
;                 const f2 xc = {XCF[(32 * tb + crow(i, hh)) * 128 + chl], XCF[(32 * tb + crow(i + 1, hh)) * 128 + chl]};
;                 const f2 ta = (f2){ya[i], ya[i + 1]} * -1.4426950408889634f, tx = (f2){yx[i], yx[i + 1]} * -1.4426950408889634f;
;                 f2 ea, ex; ea.x = __builtin_amdgcn_exp2f(ta.x); ea.y = __builtin_amdgcn_exp2f(ta.y); ex.x = __builtin_amdgcn_exp2f(tx.x); ex.y = __builtin_amdgcn_exp2f(tx.y);
;                 const f2 da = ea + 1.0f, dx = ex + 1.0f;
;                 f2 rg, ig; rg.x = __builtin_amdgcn_rcpf(da.x); rg.y = __builtin_amdgcn_rcpf(da.y); ig.x = __builtin_amdgcn_rcpf(dx.x); ig.y = __builtin_amdgcn_rcpf(dx.y);
;                 const f2 la = rg * sp8; f2 a; a.x = __builtin_amdgcn_exp2f(la.x); a.y = __builtin_amdgcn_exp2f(la.y);
;                 const f2 om = a * -a + 1.0f; f2 sq; sq.x = __builtin_amdgcn_sqrtf(om.x); sq.y = __builtin_amdgcn_sqrtf(om.y);
;                 const f2 b = sq * ig * xc;
;                 av[i] = a.x; av[i + 1] = a.y; bv[i] = b.x; bv[i + 1] = b.y; }
.LBB0_1410:
	v_and_b32_e32 v35, 64, v184
	v_xor_b32_e32 v34, 32, v184
	v_add_u32_e32 v35, 64, v35
	v_cmp_lt_i32_e32 vcc, v34, v35
	s_mov_b64 s[6:7], -1
	s_nop 0
	v_cndmask_b32_e32 v34, v184, v34, vcc
	v_lshlrev_b32_e32 v155, 2, v34
	s_and_b64 vcc, exec, s[16:17]
	s_cbranch_vccz .LBB0_1441
	s_nop 0
	ds_read_b128 v[170:173], v185 offset:8704
	ds_read_b128 v[188:191], v185 offset:8736
	s_waitcnt lgkmcnt(1)
	v_mfma_f32_32x32x16_bf16 v[50:65], v[170:173], v[66:69], v[2:17]
	v_mfma_f32_32x32x16_bf16 v[34:49], v[170:173], v[98:101], v[18:33]
	s_waitcnt lgkmcnt(0)
	v_mfma_f32_32x32x16_bf16 v[50:65], v[188:191], v[70:73], v[50:65]
	v_mfma_f32_32x32x16_bf16 v[34:49], v[188:191], v[102:105], v[34:49]
	ds_read_b128 v[170:173], v185 offset:8768
	ds_read_b128 v[188:191], v185 offset:8800
	s_waitcnt lgkmcnt(1)
	v_mfma_f32_32x32x16_bf16 v[50:65], v[170:173], v[74:77], v[50:65]
	v_mfma_f32_32x32x16_bf16 v[34:49], v[170:173], v[106:109], v[34:49]
	s_waitcnt lgkmcnt(0)
	v_mfma_f32_32x32x16_bf16 v[50:65], v[188:191], v[78:81], v[50:65]
	v_mfma_f32_32x32x16_bf16 v[34:49], v[188:191], v[110:113], v[34:49]
	ds_read_b128 v[170:173], v185 offset:8832
	ds_read_b128 v[188:191], v185 offset:8864
	s_waitcnt lgkmcnt(1)
	v_mfma_f32_32x32x16_bf16 v[50:65], v[170:173], v[82:85], v[50:65]
	v_mfma_f32_32x32x16_bf16 v[34:49], v[170:173], v[114:117], v[34:49]
	s_waitcnt lgkmcnt(0)
	v_mfma_f32_32x32x16_bf16 v[50:65], v[188:191], v[86:89], v[50:65]
	v_mfma_f32_32x32x16_bf16 v[34:49], v[188:191], v[118:121], v[34:49]
	ds_read_b128 v[170:173], v185 offset:8896
	ds_read_b128 v[188:191], v185 offset:8928
	ds_read2st64_b32 v[192:193], v186 offset0:168 offset1:170
	ds_read2st64_b32 v[196:197], v186 offset0:180 offset1:182
	s_waitcnt lgkmcnt(3)
	v_mfma_f32_32x32x16_bf16 v[50:65], v[170:173], v[90:93], v[50:65]
	s_waitcnt lgkmcnt(2)
	v_mfma_f32_32x32x16_bf16 v[50:65], v[188:191], v[94:97], v[50:65]
	v_mfma_f32_32x32x16_bf16 v[34:49], v[170:173], v[122:125], v[34:49]
	s_nop 10
	v_mul_f32_e64 v50, v50, s20
	v_mul_f32_e64 v51, v51, s20
	v_mul_f32_e64 v56, v56, s20
	v_mul_f32_e64 v57, v57, s20
	v_exp_f32_e32 v50, v50
	v_exp_f32_e32 v51, v51
	v_exp_f32_e32 v56, v56
	v_exp_f32_e32 v57, v57
	v_pk_mul_f32 v[54:55], v[54:55], s[20:21] op_sel_hi:[1,0]
	v_pk_add_f32 v[50:51], v[50:51], 1.0 op_sel_hi:[1,0]
	v_mfma_f32_32x32x16_bf16 v[34:49], v[188:191], v[126:129], v[34:49]
	v_rcp_f32_e32 v172, v50
	v_rcp_f32_e32 v173, v51
	v_pk_mul_f32 v[50:51], v[52:53], s[20:21] op_sel_hi:[1,0]
	v_pk_add_f32 v[56:57], v[56:57], 1.0 op_sel_hi:[1,0]
	v_exp_f32_e32 v52, v50
	v_exp_f32_e32 v53, v51
	v_rcp_f32_e32 v56, v56
	s_nop 4
	v_pk_mul_f32 v[34:35], v[34:35], s[20:21] op_sel_hi:[1,0]
	v_pk_mul_f32 v[36:37], v[36:37], s[20:21] op_sel_hi:[1,0]
	v_pk_add_f32 v[52:53], v[52:53], 1.0 op_sel_hi:[1,0]
	v_exp_f32_e32 v170, v34
	v_rcp_f32_e32 v52, v52
	v_rcp_f32_e32 v53, v53
	v_exp_f32_e32 v171, v35
	v_exp_f32_e32 v36, v36
	v_exp_f32_e32 v37, v37
	v_pk_mul_f32 v[52:53], v[164:165], v[52:53]
	v_pk_add_f32 v[170:171], v[170:171], 1.0 op_sel_hi:[1,0]
	v_exp_f32_e32 v52, v52
	v_exp_f32_e32 v53, v53
	v_pk_add_f32 v[36:37], v[36:37], 1.0 op_sel_hi:[1,0]
	v_rcp_f32_e32 v50, v170
	v_rcp_f32_e32 v51, v171
	v_pk_mul_f32 v[170:171], v[164:165], v[172:173]
	v_rcp_f32_e32 v172, v36
	v_rcp_f32_e32 v173, v37
	v_pk_fma_f32 v[36:37], v[52:53], v[52:53], 1.0 op_sel_hi:[1,1,0] neg_lo:[1,0,0] neg_hi:[1,0,0]
	v_rcp_f32_e32 v57, v57
	v_sqrt_f32_e32 v174, v36
	v_sqrt_f32_e32 v175, v37
	v_exp_f32_e32 v36, v170
	v_exp_f32_e32 v37, v171
	ds_read2st64_b32 v[170:171], v186 offset0:136 offset1:138
	v_pk_mul_f32 v[38:39], v[38:39], s[20:21] op_sel_hi:[1,0]
	v_pk_mul_f32 v[40:41], v[40:41], s[20:21] op_sel_hi:[1,0]
	v_pk_mul_f32 v[56:57], v[164:165], v[56:57]
	v_pk_mul_f32 v[172:173], v[172:173], v[174:175]
	v_exp_f32_e32 v174, v54
	v_exp_f32_e32 v175, v55
	v_exp_f32_e32 v38, v38
	v_exp_f32_e32 v39, v39
	v_exp_f32_e32 v40, v40
	v_exp_f32_e32 v41, v41
	v_exp_f32_e32 v56, v56
	v_exp_f32_e32 v57, v57
	s_waitcnt lgkmcnt(0)
	v_pk_mul_f32 v[170:171], v[170:171], v[172:173]
	v_pk_add_f32 v[172:173], v[174:175], 1.0 op_sel_hi:[1,0]
	v_pk_add_f32 v[38:39], v[38:39], 1.0 op_sel_hi:[1,0]
	v_pk_add_f32 v[40:41], v[40:41], 1.0 op_sel_hi:[1,0]
	v_pk_fma_f32 v[188:189], v[56:57], v[56:57], 1.0 op_sel_hi:[1,1,0] neg_lo:[1,0,0] neg_hi:[1,0,0]
	v_rcp_f32_e32 v172, v172
	v_rcp_f32_e32 v173, v173
	v_rcp_f32_e32 v174, v38
	v_rcp_f32_e32 v175, v39
	ds_read2st64_b32 v[38:39], v186 offset0:152 offset1:154
	v_rcp_f32_e32 v40, v40
	v_rcp_f32_e32 v41, v41
	v_sqrt_f32_e32 v188, v188
	v_sqrt_f32_e32 v189, v189
	v_pk_mul_f32 v[172:173], v[164:165], v[172:173]
	ds_read2st64_b32 v[34:35], v186 offset0:132 offset1:134
	v_exp_f32_e32 v191, v172
	v_pk_mul_f32 v[40:41], v[40:41], v[188:189]
	v_exp_f32_e32 v190, v173
	s_waitcnt lgkmcnt(1)
; template <bool FINAL, int z> __device__ __forceinline__ void rglru_blocks(LAS unsigned char* XCB, LAS float* XCF, LAS float* HS, const bf16x8 (&wa)[8], const bf16x8 (&wx)[8],
;         float ba, float bxx, float sp8, int r, int hh, int chl, float& st, float& CA, float& CB) {
;     ...
;             float Ag[4], Bg[4], Ap[4], Bp[4];
; #pragma unroll
;             for (int g = 0; g < 4; ++g) { float A = 1.f, B = 0.f;
; #pragma unroll
;                 for (int k = 0; k < 4; ++k) { const int kk = z ? 3 - k : k; B = B * av[4 * g + kk] + bv[4 * g + kk]; A *= av[4 * g + kk]; }
;                 Ag[g] = A; Bg[g] = B; Ap[g] = __shfl_xor(A, 32); Bp[g] = __shfl_xor(B, 32); }
;             float ent[4]; float cur = st;
; #pragma unroll
;             for (int gi = 0; gi < 4; ++gi) { const int g = z ? 3 - gi : gi;
;                 const bool own_first = z ? (hh == 1) : (hh == 0);
;                 if (own_first) { ent[g] = cur; cur = Ag[g] * cur + Bg[g]; CB = Ag[g] * CB + Bg[g]; CA *= Ag[g]; cur = Ap[g] * cur + Bp[g]; CB = Ap[g] * CB + Bp[g]; CA *= Ap[g]; }
;                 else { cur = Ap[g] * cur + Bp[g]; CB = Ap[g] * CB + Bp[g]; CA *= Ap[g]; ent[g] = cur; cur = Ag[g] * cur + Bg[g]; CB = Ag[g] * CB + Bg[g]; CA *= Ag[g]; } }
	v_pk_mul_f32 v[172:173], v[38:39], v[40:41]
	v_pk_mul_f32 v[38:39], v[58:59], s[20:21] op_sel_hi:[1,0]
	v_pk_mul_f32 v[40:41], v[42:43], s[20:21] op_sel_hi:[1,0]
	v_exp_f32_e32 v38, v38
	v_exp_f32_e32 v39, v39
	v_exp_f32_e32 v40, v40
	v_exp_f32_e32 v41, v41
	v_pk_mul_f32 v[42:43], v[44:45], s[20:21] op_sel_hi:[1,0]
	v_pk_add_f32 v[38:39], v[38:39], 1.0 op_sel_hi:[1,0]
	v_exp_f32_e32 v42, v42
	v_rcp_f32_e32 v38, v38
	v_rcp_f32_e32 v39, v39
	v_pk_add_f32 v[40:41], v[40:41], 1.0 op_sel_hi:[1,0]
	v_exp_f32_e32 v43, v43
	v_rcp_f32_e32 v58, v40
	v_rcp_f32_e32 v59, v41
	v_pk_mul_f32 v[40:41], v[164:165], v[38:39]
	v_pk_add_f32 v[42:43], v[42:43], 1.0 op_sel_hi:[1,0]
	v_exp_f32_e32 v39, v40
	v_exp_f32_e32 v38, v41
	v_pk_mul_f32 v[40:41], v[60:61], s[20:21] op_sel_hi:[1,0]
	v_rcp_f32_e32 v60, v42
	v_exp_f32_e32 v40, v40
	v_exp_f32_e32 v41, v41
	v_rcp_f32_e32 v61, v43
	v_pk_mul_f32 v[42:43], v[62:63], s[20:21] op_sel_hi:[1,0]
	v_pk_mul_f32 v[44:45], v[46:47], s[20:21] op_sel_hi:[1,0]
	v_pk_add_f32 v[40:41], v[40:41], 1.0 op_sel_hi:[1,0]
	v_exp_f32_e32 v42, v42
	v_rcp_f32_e32 v40, v40
	v_rcp_f32_e32 v41, v41
	v_exp_f32_e32 v43, v43
	v_exp_f32_e32 v44, v44
	v_exp_f32_e32 v45, v45
	v_pk_mul_f32 v[40:41], v[164:165], v[40:41]
	v_pk_mul_f32 v[46:47], v[48:49], s[20:21] op_sel_hi:[1,0]
	v_exp_f32_e32 v194, v40
	v_exp_f32_e32 v63, v41
	v_pk_add_f32 v[40:41], v[42:43], 1.0 op_sel_hi:[1,0]
	v_pk_add_f32 v[42:43], v[44:45], 1.0 op_sel_hi:[1,0]
	v_pk_mul_f32 v[44:45], v[64:65], s[20:21] op_sel_hi:[1,0]
	v_exp_f32_e32 v46, v46
	v_exp_f32_e32 v44, v44
	v_exp_f32_e32 v45, v45
	v_exp_f32_e32 v47, v47
	v_rcp_f32_e32 v40, v40
	v_rcp_f32_e32 v41, v41
	v_pk_add_f32 v[44:45], v[44:45], 1.0 op_sel_hi:[1,0]
	v_rcp_f32_e32 v64, v42
	v_rcp_f32_e32 v44, v44
	v_rcp_f32_e32 v45, v45
	v_rcp_f32_e32 v65, v43
	ds_read2st64_b32 v[42:43], v186 offset0:184 offset1:186
	v_pk_mul_f32 v[40:41], v[164:165], v[40:41]
	v_pk_mul_f32 v[44:45], v[164:165], v[44:45]
	v_exp_f32_e32 v198, v40
	v_exp_f32_e32 v48, v44
	v_exp_f32_e32 v49, v45
	v_pk_add_f32 v[44:45], v[46:47], 1.0 op_sel_hi:[1,0]
	v_exp_f32_e32 v62, v41
	v_rcp_f32_e32 v44, v44
	v_pk_fma_f32 v[46:47], v[48:49], v[48:49], 1.0 op_sel_hi:[1,1,0] neg_lo:[1,0,0] neg_hi:[1,0,0]
	v_rcp_f32_e32 v45, v45
	v_sqrt_f32_e32 v46, v46
	v_sqrt_f32_e32 v47, v47
	ds_read2st64_b32 v[54:55], v186 offset0:148 offset1:150
	v_mov_b32_e32 v195, v63
	ds_read2st64_b32 v[188:189], v186 offset0:164 offset1:166
	v_pk_mul_f32 v[40:41], v[44:45], v[46:47]
	v_mov_b32_e32 v199, v38
	s_waitcnt lgkmcnt(2)
	v_pk_mul_f32 v[200:201], v[42:43], v[40:41]
	v_pk_fma_f32 v[40:41], v[36:37], v[36:37], 1.0 op_sel_hi:[1,1,0] neg_lo:[1,0,0] neg_hi:[1,0,0]
	v_fma_f32 v42, 0, v53, v171
	v_sqrt_f32_e32 v40, v40
	v_sqrt_f32_e32 v41, v41
	v_fmac_f32_e32 v170, v52, v42
	v_mul_f32_e32 v43, v53, v52
	v_pk_mul_f32 v[40:41], v[50:51], v[40:41]
	s_nop 0
	v_pk_mul_f32 v[40:41], v[34:35], v[40:41]
	s_nop 0
	v_fma_f32 v42, v37, v170, v41
	v_mov_b32_e32 v41, v36
	v_pk_mul_f32 v[44:45], v[36:37], v[42:43]
	v_pk_fma_f32 v[34:35], v[36:37], v[42:43], v[40:41]
	v_pk_fma_f32 v[42:43], v[190:191], v[190:191], 1.0 op_sel_hi:[1,1,0] neg_lo:[1,0,0] neg_hi:[1,0,0]
	v_pk_mul_f32 v[40:41], v[40:41], v[44:45]
	v_sqrt_f32_e32 v44, v43
	v_sqrt_f32_e32 v45, v42
	v_fma_f32 v35, 0, v57, v173
	v_fmac_f32_e32 v172, v56, v35
	v_mul_f32_e32 v42, v57, v56
	v_pk_mul_f32 v[44:45], v[174:175], v[44:45]
	v_fma_f32 v35, 0, v49, v201
	s_waitcnt lgkmcnt(1)
	v_pk_mul_f32 v[44:45], v[54:55], v[44:45]
	v_mov_b32_e32 v54, v198
	v_fma_f32 v43, v190, v172, v45
	v_pk_mul_f32 v[46:47], v[190:191], v[42:43]
	v_pk_mov_b32 v[50:51], v[190:191], v[44:45] op_sel:[1,0]
	v_mov_b32_e32 v55, v62
	v_pk_fma_f32 v[44:45], v[190:191], v[42:43], v[50:51]
	v_pk_mul_f32 v[46:47], v[50:51], v[46:47]
	v_pk_fma_f32 v[50:51], v[38:39], v[38:39], 1.0 op_sel_hi:[1,1,0] neg_lo:[1,0,0] neg_hi:[1,0,0]
	v_pk_fma_f32 v[54:55], v[54:55], v[54:55], 1.0 op_sel_hi:[1,1,0] neg_lo:[1,0,0] neg_hi:[1,0,0]
	v_sqrt_f32_e32 v52, v51
	v_sqrt_f32_e32 v53, v50
	v_sqrt_f32_e32 v54, v54
	v_sqrt_f32_e32 v55, v55
	v_fmac_f32_e32 v200, v48, v35
	v_pk_mul_f32 v[50:51], v[58:59], v[52:53]
	v_pk_fma_f32 v[52:53], v[194:195], v[194:195], 1.0 op_sel_hi:[1,1,0] neg_lo:[1,0,0] neg_hi:[1,0,0]
	s_waitcnt lgkmcnt(0)
	v_pk_mul_f32 v[56:57], v[188:189], v[50:51]
	v_sqrt_f32_e32 v52, v52
	v_sqrt_f32_e32 v53, v53
	v_mul_f32_e32 v48, v49, v48
	v_mov_b32_e32 v49, v194
	v_pk_mul_f32 v[48:49], v[62:63], v[48:49]
	v_pk_mul_f32 v[50:51], v[60:61], v[52:53]
	v_pk_mul_f32 v[60:61], v[198:199], v[48:49]
	v_pk_mul_f32 v[52:53], v[192:193], v[50:51]
	v_pk_mul_f32 v[50:51], v[64:65], v[54:55]
	v_fma_f32 v35, 0, v63, v53
	v_fmac_f32_e32 v52, v194, v35
	v_pk_mul_f32 v[50:51], v[196:197], v[50:51]
	v_fma_f32 v53, v38, v52, v57
	v_mov_b32_e32 v52, v49
	v_pk_mul_f32 v[54:55], v[38:39], v[52:53]
	v_pk_mov_b32 v[48:49], v[38:39], v[56:57] op_sel:[1,0]
	v_fma_f32 v35, v62, v200, v51
	v_pk_fma_f32 v[56:57], v[38:39], v[52:53], v[48:49]
	v_pk_mul_f32 v[52:53], v[48:49], v[54:55]
	ds_bpermute_b32 v38, v155, v60
	v_fmac_f32_e32 v50, v198, v35
	ds_bpermute_b32 v37, v155, v41
	ds_bpermute_b32 v36, v155, v34
	ds_bpermute_b32 v42, v155, v46
	ds_bpermute_b32 v43, v155, v45
	ds_bpermute_b32 v54, v155, v52
	ds_bpermute_b32 v55, v155, v57
	ds_bpermute_b32 v35, v155, v50
	v_mov_b32_e32 v53, v57
	s_waitcnt lgkmcnt(7)
	v_pk_mul_f32 v[58:59], v[38:39], v[60:61]
	s_and_saveexec_b64 s[6:7], s[0:1]
	s_xor_b64 s[6:7], exec, s[6:7]
	s_cbranch_execz .LBB0_1413
	s_waitcnt lgkmcnt(0)
	v_fmac_f32_e32 v35, 0, v38
	v_fmac_f32_e32 v50, v60, v35
	v_mov_b32_e32 v39, v55
	v_fmac_f32_e32 v39, v50, v54
	v_mov_b32_e32 v38, v54
	v_pk_mul_f32 v[50:51], v[58:59], v[54:55]
	v_pk_fma_f32 v[48:49], v[58:59], v[38:39], v[52:53]
	s_nop 0
	v_mul_f32_e32 v48, v52, v50

; template <bool FINAL, int z> __device__ __forceinline__ void rglru_blocks(LAS unsigned char* XCB, LAS float* XCF, LAS float* HS, const bf16x8 (&wa)[8], const bf16x8 (&wx)[8],
;         float ba, float bxx, float sp8, int r, int hh, int chl, float& st, float& CA, float& CB) {
;     ...
;             if (z == 1 && bi == 0) __builtin_amdgcn_s_sleep(8);
;             f32x16 ya, yx;
; #pragma unroll
;             for (int i = 0; i < 16; ++i) { ya[i] = ba; yx[i] = bxx; }
; #pragma unroll
;             for (int s = 0; s < 8; ++s) { const bf16x8 af = *(const LAS bf16x8*)(XCB + (32 * tb + r) * 272 + (16 * s + 8 * hh) * 2);
;                 ya = __builtin_amdgcn_mfma_f32_32x32x16_bf16(af, wa[s], ya, 0, 0, 0); yx = __builtin_amdgcn_mfma_f32_32x32x16_bf16(af, wx[s], yx, 0, 0, 0); }
;             float av[16], bv[16];
; #pragma unroll
;             for (int i = 0; i < 16; i += 2) {
;                 typedef float f2 __attribute__((ext_vector_type(2)));
;                 const f2 xc = {XCF[(32 * tb + crow(i, hh)) * 128 + chl], XCF[(32 * tb + crow(i + 1, hh)) * 128 + chl]};
;                 const f2 ta = (f2){ya[i], ya[i + 1]} * -1.4426950408889634f, tx = (f2){yx[i], yx[i + 1]} * -1.4426950408889634f;
;                 f2 ea, ex; ea.x = __builtin_amdgcn_exp2f(ta.x); ea.y = __builtin_amdgcn_exp2f(ta.y); ex.x = __builtin_amdgcn_exp2f(tx.x); ex.y = __builtin_amdgcn_exp2f(tx.y);
;                 const f2 da = ea + 1.0f, dx = ex + 1.0f;
;                 f2 rg, ig; rg.x = __builtin_amdgcn_rcpf(da.x); rg.y = __builtin_amdgcn_rcpf(da.y); ig.x = __builtin_amdgcn_rcpf(dx.x); ig.y = __builtin_amdgcn_rcpf(dx.y);
;                 const f2 la = rg * sp8; f2 a; a.x = __builtin_amdgcn_exp2f(la.x); a.y = __builtin_amdgcn_exp2f(la.y);
; template <bool FINAL> __device__ __forceinline__ void rglru_pass(Frame& F) {
;     ...
;         v4u gq[2];
;         if (FINAL) {
; #pragma unroll
;             for (int it = 0; it < 2; ++it) { const int id = F.tid + 512 * it; gq[it] = *(const GAS v4u*)(Z1 + (size_t)(row0 + (id >> 4)) * 4096 + h * 128 + (id & 15) * 8); } }
;         float st = 0.f, CA = 1.f, CB = 0.f;
;         if (FINAL) st = CL[((c - cg) / ncg) * 256 + z * 128 + chl];
;         if (z == 0) rglru_blocks<FINAL, 0>(XCB, XCF, HS, wa, wx, ba, bxx, sp8, r, hh, chl, st, CA, CB);
;         else rglru_blocks<FINAL, 1>(XCB, XCF, HS, wa, wx, ba, bxx, sp8, r, hh, chl, st, CA, CB);
.LBB0_1603:
	v_add_u32_e32 v192, s15, v174
	v_ashrrev_i32_e32 v193, 31, v192
	v_add_u32_e32 v190, s15, v176
	v_lshlrev_b64 v[34:35], 13, v[192:193]
	v_ashrrev_i32_e32 v191, 31, v190
	v_lshl_add_u64 v[34:35], v[188:189], 0, v[34:35]
	v_lshlrev_b64 v[36:37], 13, v[190:191]
	v_lshl_add_u64 v[36:37], v[188:189], 0, v[36:37]
	global_load_dwordx4 v[168:171], v[34:35], off
	global_load_dwordx4 v[164:167], v[36:37], off
	s_abs_i32 s5, s22
	s_mul_hi_u32 s23, s5, s16
	s_mul_i32 s24, s23, s13
	s_ashr_i32 s4, s22, 31
	s_sub_i32 s5, s5, s24
	s_xor_b32 s4, s4, s14
	s_add_i32 s24, s23, 1
	s_sub_i32 s25, s5, s13
	s_cmp_ge_u32 s5, s13
	s_cselect_b32 s23, s24, s23
	s_cselect_b32 s5, s25, s5
	s_add_i32 s24, s23, 1
	s_cmp_ge_u32 s5, s13
	s_cselect_b32 s5, s24, s23
	s_xor_b32 s5, s5, s4
	s_sub_i32 s4, s5, s4
	v_lshl_add_u32 v34, s4, 10, v1
	ds_read_b32 v209, v34
	v_and_b32_e32 v35, 64, v203
	v_xor_b32_e32 v34, 32, v203
	v_add_u32_e32 v35, 64, v35
	v_cmp_lt_i32_e32 vcc, v34, v35
	s_mov_b64 s[4:5], -1
	s_nop 0
	v_cndmask_b32_e32 v34, v203, v34, vcc
	v_lshlrev_b32_e32 v159, 2, v34
	s_and_b64 vcc, exec, s[8:9]
	s_cbranch_vccz .LBB0_1605
	s_nop 0
	ds_read_b128 v[210:213], v208 offset:8704
	ds_read_b128 v[214:217], v208 offset:8736
	s_mov_b64 s[4:5], 0
	s_waitcnt lgkmcnt(1)
	v_mfma_f32_32x32x16_bf16 v[50:65], v[210:213], v[66:69], v[2:17]
	v_mfma_f32_32x32x16_bf16 v[34:49], v[210:213], v[98:101], v[18:33]
	s_waitcnt lgkmcnt(0)
	v_mfma_f32_32x32x16_bf16 v[50:65], v[214:217], v[70:73], v[50:65]
	v_mfma_f32_32x32x16_bf16 v[34:49], v[214:217], v[102:105], v[34:49]
	ds_read_b128 v[210:213], v208 offset:8768
	ds_read_b128 v[214:217], v208 offset:8800
	s_waitcnt lgkmcnt(1)
	v_mfma_f32_32x32x16_bf16 v[50:65], v[210:213], v[74:77], v[50:65]
	v_mfma_f32_32x32x16_bf16 v[34:49], v[210:213], v[106:109], v[34:49]
	s_waitcnt lgkmcnt(0)
	v_mfma_f32_32x32x16_bf16 v[50:65], v[214:217], v[78:81], v[50:65]
	v_mfma_f32_32x32x16_bf16 v[34:49], v[214:217], v[110:113], v[34:49]
	ds_read_b128 v[210:213], v208 offset:8832
	ds_read_b128 v[214:217], v208 offset:8864
	s_waitcnt lgkmcnt(1)
	v_mfma_f32_32x32x16_bf16 v[50:65], v[210:213], v[82:85], v[50:65]
	v_mfma_f32_32x32x16_bf16 v[34:49], v[210:213], v[114:117], v[34:49]
	s_waitcnt lgkmcnt(0)
	v_mfma_f32_32x32x16_bf16 v[50:65], v[214:217], v[86:89], v[50:65]
	v_mfma_f32_32x32x16_bf16 v[34:49], v[214:217], v[118:121], v[34:49]
	ds_read_b128 v[210:213], v208 offset:8896
	ds_read_b128 v[214:217], v208 offset:8928
	s_waitcnt lgkmcnt(1)
	v_mfma_f32_32x32x16_bf16 v[50:65], v[210:213], v[90:93], v[50:65]
	s_waitcnt lgkmcnt(0)
	v_mfma_f32_32x32x16_bf16 v[50:65], v[214:217], v[94:97], v[50:65]
	v_mfma_f32_32x32x16_bf16 v[34:49], v[210:213], v[122:125], v[34:49]
	s_nop 10
	v_mul_f32_e64 v50, v50, s12
	v_mul_f32_e64 v51, v51, s12
	v_mul_f32_e64 v54, v54, s12
	v_mul_f32_e64 v55, v55, s12
	v_exp_f32_e32 v50, v50
	v_exp_f32_e32 v51, v51
	v_pk_mul_f32 v[52:53], v[52:53], s[12:13] op_sel_hi:[1,0]
	v_exp_f32_e32 v54, v54
	v_exp_f32_e32 v55, v55
	v_mfma_f32_32x32x16_bf16 v[34:49], v[214:217], v[126:129], v[34:49]
	v_add_f32_e64 v50, v50, 1.0
	v_add_f32_e64 v51, v51, 1.0
	v_exp_f32_e32 v52, v52
	v_rcp_f32_e32 v50, v50
	v_rcp_f32_e32 v51, v51
	v_exp_f32_e32 v53, v53
	v_pk_add_f32 v[54:55], v[54:55], 1.0 op_sel_hi:[1,0]
	ds_read2st64_b32 v[210:211], v175 offset0:132 offset1:134
	s_nop 3
	v_pk_mul_f32 v[34:35], v[34:35], s[12:13] op_sel_hi:[1,0]
	v_pk_add_f32 v[52:53], v[52:53], 1.0 op_sel_hi:[1,0]
	v_exp_f32_e32 v212, v34
	v_exp_f32_e32 v213, v35
	v_pk_mul_f32 v[34:35], v[182:183], v[50:51]
	v_rcp_f32_e32 v54, v54
	v_exp_f32_e32 v34, v34
	v_exp_f32_e32 v35, v35
	v_pk_add_f32 v[50:51], v[212:213], 1.0 op_sel_hi:[1,0]
	v_rcp_f32_e32 v55, v55
	v_rcp_f32_e32 v50, v50
	v_pk_fma_f32 v[212:213], v[34:35], v[34:35], 1.0 op_sel_hi:[1,1,0] neg_lo:[1,0,0] neg_hi:[1,0,0]
	v_rcp_f32_e32 v51, v51
	v_sqrt_f32_e32 v212, v212
	v_sqrt_f32_e32 v213, v213
	v_rcp_f32_e32 v52, v52
	v_rcp_f32_e32 v53, v53
	v_pk_mul_f32 v[38:39], v[38:39], s[12:13] op_sel_hi:[1,0]
	v_pk_mul_f32 v[50:51], v[50:51], v[212:213]
	v_pk_mul_f32 v[36:37], v[36:37], s[12:13] op_sel_hi:[1,0]
	v_exp_f32_e32 v214, v38
	v_exp_f32_e32 v215, v39
	v_pk_mul_f32 v[38:39], v[182:183], v[54:55]
	s_waitcnt lgkmcnt(0)
	v_pk_mul_f32 v[50:51], v[210:211], v[50:51]
	v_exp_f32_e32 v210, v36
	v_exp_f32_e32 v211, v37
	v_pk_mul_f32 v[36:37], v[182:183], v[52:53]
	v_exp_f32_e32 v38, v38
	v_exp_f32_e32 v39, v39
	v_exp_f32_e32 v36, v36
	v_exp_f32_e32 v37, v37
	v_pk_add_f32 v[54:55], v[214:215], 1.0 op_sel_hi:[1,0]
	v_pk_add_f32 v[52:53], v[210:211], 1.0 op_sel_hi:[1,0]
	v_rcp_f32_e32 v214, v54
	v_rcp_f32_e32 v215, v55
	v_pk_fma_f32 v[54:55], v[38:39], v[38:39], 1.0 op_sel_hi:[1,1,0] neg_lo:[1,0,0] neg_hi:[1,0,0]
	v_pk_fma_f32 v[210:211], v[36:37], v[36:37], 1.0 op_sel_hi:[1,1,0] neg_lo:[1,0,0] neg_hi:[1,0,0]
	v_sqrt_f32_e32 v216, v54
	v_sqrt_f32_e32 v217, v55
	v_pk_mul_f32 v[54:55], v[56:57], s[12:13] op_sel_hi:[1,0]
	v_rcp_f32_e32 v52, v52
	v_rcp_f32_e32 v53, v53
	v_sqrt_f32_e32 v210, v210
	v_sqrt_f32_e32 v211, v211
	v_exp_f32_e32 v56, v54
	v_exp_f32_e32 v57, v55
	ds_read2st64_b32 v[212:213], v175 offset0:136 offset1:138
	v_pk_mul_f32 v[58:59], v[58:59], s[12:13] op_sel_hi:[1,0]
	v_pk_mul_f32 v[52:53], v[52:53], v[210:211]
	ds_read2st64_b32 v[210:211], v175 offset0:148 offset1:150
	v_pk_add_f32 v[56:57], v[56:57], 1.0 op_sel_hi:[1,0]
	v_exp_f32_e32 v58, v58
	v_exp_f32_e32 v59, v59
	v_rcp_f32_e32 v56, v56
	v_rcp_f32_e32 v57, v57
	s_waitcnt lgkmcnt(1)
	v_pk_mul_f32 v[54:55], v[212:213], v[52:53]
	v_pk_mul_f32 v[52:53], v[214:215], v[216:217]
	v_pk_mul_f32 v[40:41], v[40:41], s[12:13] op_sel_hi:[1,0]
	v_pk_add_f32 v[58:59], v[58:59], 1.0 op_sel_hi:[1,0]
	s_waitcnt lgkmcnt(0)
; __device__ __forceinline__ int crow(int r, int hh) { return (r & 3) + 8 * (r >> 2) + 4 * hh; }
; template <bool FINAL, int z> __device__ __forceinline__ void rglru_blocks(LAS unsigned char* XCB, LAS float* XCF, LAS float* HS, const bf16x8 (&wa)[8], const bf16x8 (&wx)[8],
;         float ba, float bxx, float sp8, int r, int hh, int chl, float& st, float& CA, float& CB) {
;     ...
;             float av[16], bv[16];
; #pragma unroll
;             for (int i = 0; i < 16; i += 2) {
;                 typedef float f2 __attribute__((ext_vector_type(2)));
;                 const f2 xc = {XCF[(32 * tb + crow(i, hh)) * 128 + chl], XCF[(32 * tb + crow(i + 1, hh)) * 128 + chl]};
;                 const f2 ta = (f2){ya[i], ya[i + 1]} * -1.4426950408889634f, tx = (f2){yx[i], yx[i + 1]} * -1.4426950408889634f;
;                 f2 ea, ex; ea.x = __builtin_amdgcn_exp2f(ta.x); ea.y = __builtin_amdgcn_exp2f(ta.y); ex.x = __builtin_amdgcn_exp2f(tx.x); ex.y = __builtin_amdgcn_exp2f(tx.y);
;                 const f2 da = ea + 1.0f, dx = ex + 1.0f;
;                 f2 rg, ig; rg.x = __builtin_amdgcn_rcpf(da.x); rg.y = __builtin_amdgcn_rcpf(da.y); ig.x = __builtin_amdgcn_rcpf(dx.x); ig.y = __builtin_amdgcn_rcpf(dx.y);
;                 const f2 la = rg * sp8; f2 a; a.x = __builtin_amdgcn_exp2f(la.x); a.y = __builtin_amdgcn_exp2f(la.y);
;                 const f2 om = a * -a + 1.0f; f2 sq; sq.x = __builtin_amdgcn_sqrtf(om.x); sq.y = __builtin_amdgcn_sqrtf(om.y);
;                 const f2 b = sq * ig * xc;
;                 av[i] = a.x; av[i + 1] = a.y; bv[i] = b.x; bv[i + 1] = b.y; }
;             float Ag[4], Bg[4], Ap[4], Bp[4];
; #pragma unroll
;             for (int g = 0; g < 4; ++g) { float A = 1.f, B = 0.f;
; #pragma unroll
;                 for (int k = 0; k < 4; ++k) { const int kk = z ? 3 - k : k; B = B * av[4 * g + kk] + bv[4 * g + kk]; A *= av[4 * g + kk]; }
;                 Ag[g] = A; Bg[g] = B; Ap[g] = __shfl_xor(A, 32); Bp[g] = __shfl_xor(B, 32); }
;             float ent[4]; float cur = st;
; #pragma unroll
;             for (int gi = 0; gi < 4; ++gi) { const int g = z ? 3 - gi : gi;
;                 const bool own_first = z ? (hh == 1) : (hh == 0);
;                 if (own_first) { ent[g] = cur; cur = Ag[g] * cur + Bg[g]; CB = Ag[g] * CB + Bg[g]; CA *= Ag[g]; cur = Ap[g] * cur + Bp[g]; CB = Ap[g] * CB + Bp[g]; CA *= Ap[g]; }
	v_pk_mul_f32 v[52:53], v[210:211], v[52:53]
	v_exp_f32_e32 v210, v40
	v_exp_f32_e32 v211, v41
	v_pk_mul_f32 v[40:41], v[182:183], v[56:57]
	v_rcp_f32_e32 v58, v58
	v_rcp_f32_e32 v59, v59
	v_pk_mul_f32 v[60:61], v[60:61], s[12:13] op_sel_hi:[1,0]
	v_exp_f32_e32 v40, v40
	v_exp_f32_e32 v41, v41
	v_exp_f32_e32 v60, v60
	v_exp_f32_e32 v61, v61
	v_pk_mul_f32 v[64:65], v[64:65], s[12:13] op_sel_hi:[1,0]
	v_pk_mul_f32 v[42:43], v[42:43], s[12:13] op_sel_hi:[1,0]
	v_exp_f32_e32 v64, v64
	v_exp_f32_e32 v65, v65
	v_exp_f32_e32 v214, v42
	v_exp_f32_e32 v215, v43
	v_pk_mul_f32 v[42:43], v[182:183], v[58:59]
	v_pk_mul_f32 v[62:63], v[62:63], s[12:13] op_sel_hi:[1,0]
	v_pk_add_f32 v[56:57], v[210:211], 1.0 op_sel_hi:[1,0]
	v_pk_fma_f32 v[210:211], v[40:41], v[40:41], 1.0 op_sel_hi:[1,1,0] neg_lo:[1,0,0] neg_hi:[1,0,0]
	v_exp_f32_e32 v42, v42
	v_exp_f32_e32 v43, v43
	v_pk_add_f32 v[60:61], v[60:61], 1.0 op_sel_hi:[1,0]
	v_exp_f32_e32 v62, v62
	v_exp_f32_e32 v63, v63
	v_rcp_f32_e32 v56, v56
	v_rcp_f32_e32 v57, v57
	v_sqrt_f32_e32 v210, v210
	v_sqrt_f32_e32 v211, v211
	v_rcp_f32_e32 v60, v60
	v_rcp_f32_e32 v61, v61
	v_pk_add_f32 v[64:65], v[64:65], 1.0 op_sel_hi:[1,0]
	v_pk_add_f32 v[58:59], v[214:215], 1.0 op_sel_hi:[1,0]
	v_rcp_f32_e32 v64, v64
	v_rcp_f32_e32 v65, v65
	v_pk_fma_f32 v[214:215], v[42:43], v[42:43], 1.0 op_sel_hi:[1,1,0] neg_lo:[1,0,0] neg_hi:[1,0,0]
	v_pk_add_f32 v[62:63], v[62:63], 1.0 op_sel_hi:[1,0]
	v_pk_mul_f32 v[56:57], v[56:57], v[210:211]
	ds_read2st64_b32 v[210:211], v175 offset0:164 offset1:166
	v_rcp_f32_e32 v58, v58
	v_rcp_f32_e32 v59, v59
	v_sqrt_f32_e32 v214, v214
	v_sqrt_f32_e32 v215, v215
	v_pk_mul_f32 v[44:45], v[44:45], s[12:13] op_sel_hi:[1,0]
	v_pk_mul_f32 v[60:61], v[182:183], v[60:61]
	v_rcp_f32_e32 v62, v62
	v_rcp_f32_e32 v63, v63
	v_exp_f32_e32 v44, v44
	v_exp_f32_e32 v45, v45
	v_exp_f32_e32 v60, v60
	v_exp_f32_e32 v61, v61
	v_pk_mul_f32 v[48:49], v[48:49], s[12:13] op_sel_hi:[1,0]
	v_pk_mul_f32 v[64:65], v[182:183], v[64:65]
	v_exp_f32_e32 v48, v48
	v_exp_f32_e32 v49, v49
	v_exp_f32_e32 v64, v64
	v_exp_f32_e32 v65, v65
	v_pk_mul_f32 v[58:59], v[58:59], v[214:215]
	v_pk_mul_f32 v[46:47], v[46:47], s[12:13] op_sel_hi:[1,0]
	v_pk_mul_f32 v[62:63], v[182:183], v[62:63]
	s_waitcnt lgkmcnt(0)
	v_pk_mul_f32 v[58:59], v[210:211], v[58:59]
	v_pk_add_f32 v[44:45], v[44:45], 1.0 op_sel_hi:[1,0]
	v_pk_fma_f32 v[210:211], v[60:61], v[60:61], 1.0 op_sel_hi:[1,1,0] neg_lo:[1,0,0] neg_hi:[1,0,0]
	v_exp_f32_e32 v46, v46
	v_exp_f32_e32 v47, v47
	v_exp_f32_e32 v62, v62
	v_exp_f32_e32 v63, v63
	v_rcp_f32_e32 v44, v44
	v_rcp_f32_e32 v45, v45
	v_sqrt_f32_e32 v210, v210
	v_sqrt_f32_e32 v211, v211
	ds_read2st64_b32 v[212:213], v175 offset0:152 offset1:154
	v_pk_add_f32 v[48:49], v[48:49], 1.0 op_sel_hi:[1,0]
	v_pk_fma_f32 v[218:219], v[64:65], v[64:65], 1.0 op_sel_hi:[1,1,0] neg_lo:[1,0,0] neg_hi:[1,0,0]
	ds_read2st64_b32 v[216:217], v175 offset0:184 offset1:186
	v_rcp_f32_e32 v48, v48
	v_rcp_f32_e32 v49, v49
	v_sqrt_f32_e32 v218, v218
	v_sqrt_f32_e32 v219, v219
	v_pk_add_f32 v[46:47], v[46:47], 1.0 op_sel_hi:[1,0]
	v_pk_fma_f32 v[214:215], v[62:63], v[62:63], 1.0 op_sel_hi:[1,1,0] neg_lo:[1,0,0] neg_hi:[1,0,0]
	v_pk_mul_f32 v[44:45], v[44:45], v[210:211]
	ds_read2st64_b32 v[210:211], v175 offset0:180 offset1:182
	v_rcp_f32_e32 v46, v46
	v_rcp_f32_e32 v47, v47
	v_sqrt_f32_e32 v214, v214
	v_sqrt_f32_e32 v215, v215
	s_waitcnt lgkmcnt(2)
	v_pk_mul_f32 v[56:57], v[212:213], v[56:57]
	ds_read2st64_b32 v[212:213], v175 offset0:168 offset1:170
	v_pk_mul_f32 v[48:49], v[48:49], v[218:219]
	v_pk_mul_f32 v[46:47], v[46:47], v[214:215]
	s_waitcnt lgkmcnt(2)
	v_pk_mul_f32 v[48:49], v[216:217], v[48:49]
	s_waitcnt lgkmcnt(1)
	v_pk_mul_f32 v[46:47], v[210:211], v[46:47]
	v_fma_f32 v218, 0, v65, v49
	v_fma_f32 v218, v64, v218, v48
	v_mul_f32_e32 v219, v65, v64
	v_fma_f32 v218, v63, v218, v47
	v_mul_f32_e32 v219, v63, v219
	s_waitcnt lgkmcnt(0)
	v_pk_mul_f32 v[44:45], v[212:213], v[44:45]
	v_fma_f32 v218, v62, v218, v46
	v_mul_f32_e32 v219, v62, v219
	v_fma_f32 v216, 0, v61, v45
	ds_bpermute_b32 v222, v159, v219
	ds_bpermute_b32 v223, v159, v218
	v_fma_f32 v210, 0, v37, v55
	v_fma_f32 v216, v60, v216, v44
	v_mul_f32_e32 v217, v61, v60
	v_fma_f32 v210, v36, v210, v54
	v_fma_f32 v216, v43, v216, v59
	v_mul_f32_e32 v217, v43, v217
	v_fma_f32 v210, v35, v210, v51
	v_fma_f32 v216, v42, v216, v58
	v_mul_f32_e32 v217, v42, v217
	v_fma_f32 v220, v34, v210, v50
	v_fma_f32 v210, 0, v41, v57
	ds_bpermute_b32 v224, v159, v217
	ds_bpermute_b32 v225, v159, v216
	v_fma_f32 v226, v209, v219, v218
	v_fma_f32 v210, v40, v210, v56
	v_mul_f32_e32 v213, v41, v40
	s_waitcnt lgkmcnt(2)
	v_fma_f32 v226, v226, v222, v223
	v_fmac_f32_e32 v223, v209, v222
	v_fma_f32 v210, v39, v210, v53
	v_mul_f32_e32 v213, v39, v213
	v_fmac_f32_e32 v218, v219, v223
	v_fma_f32 v210, v38, v210, v52
	v_mul_f32_e32 v213, v38, v213
	v_cndmask_b32_e64 v218, v218, v226, s[0:1]
	ds_bpermute_b32 v214, v159, v213
	ds_bpermute_b32 v215, v159, v210
	v_fma_f32 v222, v217, v218, v216
	v_mul_f32_e32 v211, v37, v36
	s_waitcnt lgkmcnt(2)
	v_fma_f32 v222, v222, v224, v225
	v_fmac_f32_e32 v225, v218, v224
	v_mul_f32_e32 v211, v35, v211
	v_fmac_f32_e32 v216, v217, v225
	v_mul_f32_e32 v211, v34, v211
	v_cndmask_b32_e64 v216, v216, v222, s[0:1]
	ds_bpermute_b32 v212, v159, v211
	ds_bpermute_b32 v221, v159, v220
	v_fma_f32 v218, v213, v216, v210
	s_waitcnt lgkmcnt(2)
	v_fma_f32 v218, v218, v214, v215
	v_fmac_f32_e32 v215, v216, v214
	v_fmac_f32_e32 v210, v213, v215
	v_cndmask_b32_e64 v214, v210, v218, s[0:1]
	v_fma_f32 v210, v211, v214, v220
	s_waitcnt lgkmcnt(0)
; template <bool FINAL, int z> __device__ __forceinline__ void rglru_blocks(LAS unsigned char* XCB, LAS float* XCF, LAS float* HS, const bf16x8 (&wa)[8], const bf16x8 (&wx)[8],
;         float ba, float bxx, float sp8, int r, int hh, int chl, float& st, float& CA, float& CB) {
;     ...
;             for (int s = 0; s < 8; ++s) { const bf16x8 af = *(const LAS bf16x8*)(XCB + (32 * tb + r) * 272 + (16 * s + 8 * hh) * 2);
;                 ya = __builtin_amdgcn_mfma_f32_32x32x16_bf16(af, wa[s], ya, 0, 0, 0); yx = __builtin_amdgcn_mfma_f32_32x32x16_bf16(af, wx[s], yx, 0, 0, 0); }
;             float av[16], bv[16];
; #pragma unroll
;             for (int i = 0; i < 16; i += 2) {
;                 typedef float f2 __attribute__((ext_vector_type(2)));
;                 const f2 xc = {XCF[(32 * tb + crow(i, hh)) * 128 + chl], XCF[(32 * tb + crow(i + 1, hh)) * 128 + chl]};
;                 const f2 ta = (f2){ya[i], ya[i + 1]} * -1.4426950408889634f, tx = (f2){yx[i], yx[i + 1]} * -1.4426950408889634f;
;                 f2 ea, ex; ea.x = __builtin_amdgcn_exp2f(ta.x); ea.y = __builtin_amdgcn_exp2f(ta.y); ex.x = __builtin_amdgcn_exp2f(tx.x); ex.y = __builtin_amdgcn_exp2f(tx.y);
;                 const f2 da = ea + 1.0f, dx = ex + 1.0f;
;                 f2 rg, ig; rg.x = __builtin_amdgcn_rcpf(da.x); rg.y = __builtin_amdgcn_rcpf(da.y); ig.x = __builtin_amdgcn_rcpf(dx.x); ig.y = __builtin_amdgcn_rcpf(dx.y);
;                 const f2 la = rg * sp8; f2 a; a.x = __builtin_amdgcn_exp2f(la.x); a.y = __builtin_amdgcn_exp2f(la.y);
;                 const f2 om = a * -a + 1.0f; f2 sq; sq.x = __builtin_amdgcn_sqrtf(om.x); sq.y = __builtin_amdgcn_sqrtf(om.y);
;                 const f2 b = sq * ig * xc;
;                 av[i] = a.x; av[i + 1] = a.y; bv[i] = b.x; bv[i + 1] = b.y; }
;             float Ag[4], Bg[4], Ap[4], Bp[4];
; #pragma unroll
;             for (int g = 0; g < 4; ++g) { float A = 1.f, B = 0.f;
; #pragma unroll
;                 for (int k = 0; k < 4; ++k) { const int kk = z ? 3 - k : k; B = B * av[4 * g + kk] + bv[4 * g + kk]; A *= av[4 * g + kk]; }
;                 Ag[g] = A; Bg[g] = B; Ap[g] = __shfl_xor(A, 32); Bp[g] = __shfl_xor(B, 32); }
;             float ent[4]; float cur = st;
; #pragma unroll
;             for (int gi = 0; gi < 4; ++gi) { const int g = z ? 3 - gi : gi;
;                 const bool own_first = z ? (hh == 1) : (hh == 0);
	v_fma_f32 v210, v210, v212, v221
	v_fmac_f32_e32 v221, v214, v212
	v_cndmask_b32_e64 v212, v221, v218, s[0:1]
	v_fma_f32 v37, v37, v212, v55
	v_fmac_f32_e32 v54, v36, v37
	v_cndmask_b32_e64 v213, v215, v222, s[0:1]
	v_fma_f32 v35, v35, v54, v51
	v_fmac_f32_e32 v50, v34, v35
	v_fma_f32 v34, v41, v213, v57
	v_fmac_f32_e32 v56, v40, v34
	ds_write2st64_b32 v177, v56, v34 offset0:212 offset1:214
	v_fma_f32 v34, v39, v56, v53
	v_cndmask_b32_e64 v217, v225, v226, s[0:1]
	v_fmac_f32_e32 v52, v38, v34
	ds_write2st64_b32 v177, v52, v34 offset0:208 offset1:210
	v_fma_f32 v34, v61, v217, v45
	v_fmac_f32_e32 v44, v60, v34
	ds_write2st64_b32 v177, v44, v34 offset0:228 offset1:230
	v_fma_f32 v34, v43, v44, v59
	v_cndmask_b32_e64 v219, v223, v209, s[0:1]
	v_fmac_f32_e32 v58, v42, v34
	ds_write2st64_b32 v177, v58, v34 offset0:224 offset1:226
	v_fma_f32 v34, v65, v219, v49
	v_fmac_f32_e32 v48, v64, v34
	ds_write2st64_b32 v177, v48, v34 offset0:244 offset1:246
	v_fma_f32 v34, v63, v48, v47
	v_fmac_f32_e32 v46, v62, v34
	ds_write2st64_b32 v177, v54, v37 offset0:196 offset1:198
	ds_write2st64_b32 v177, v50, v35 offset0:192 offset1:194
	ds_write2st64_b32 v177, v46, v34 offset0:240 offset1:242
	ds_read_b128 v[212:215], v208
	ds_read_b128 v[216:219], v208 offset:32
	s_waitcnt lgkmcnt(1)
	v_mfma_f32_32x32x16_bf16 v[50:65], v[212:215], v[66:69], v[2:17]
	v_fmac_f32_e32 v220, v211, v221
	v_cndmask_b32_e64 v211, v220, v210, s[0:1]
	v_mfma_f32_32x32x16_bf16 v[34:49], v[212:215], v[98:101], v[18:33]
	s_waitcnt lgkmcnt(0)
	v_mfma_f32_32x32x16_bf16 v[50:65], v[216:219], v[70:73], v[50:65]
	v_mfma_f32_32x32x16_bf16 v[34:49], v[216:219], v[102:105], v[34:49]
	ds_read_b128 v[212:215], v208 offset:64
	ds_read_b128 v[216:219], v208 offset:96
	s_waitcnt lgkmcnt(1)
	v_mfma_f32_32x32x16_bf16 v[50:65], v[212:215], v[74:77], v[50:65]
	v_mfma_f32_32x32x16_bf16 v[34:49], v[212:215], v[106:109], v[34:49]
	s_waitcnt lgkmcnt(0)
	v_mfma_f32_32x32x16_bf16 v[50:65], v[216:219], v[78:81], v[50:65]
	v_mfma_f32_32x32x16_bf16 v[34:49], v[216:219], v[110:113], v[34:49]
	ds_read_b128 v[212:215], v208 offset:128
	ds_read_b128 v[216:219], v208 offset:160
	s_waitcnt lgkmcnt(1)
	v_mfma_f32_32x32x16_bf16 v[50:65], v[212:215], v[82:85], v[50:65]
	v_mfma_f32_32x32x16_bf16 v[34:49], v[212:215], v[114:117], v[34:49]
	s_waitcnt lgkmcnt(0)
	v_mfma_f32_32x32x16_bf16 v[50:65], v[216:219], v[86:89], v[50:65]
	v_mfma_f32_32x32x16_bf16 v[34:49], v[216:219], v[118:121], v[34:49]
	ds_read_b128 v[212:215], v208 offset:192
	ds_read_b128 v[216:219], v208 offset:224
	s_waitcnt lgkmcnt(1)
	v_mfma_f32_32x32x16_bf16 v[50:65], v[212:215], v[90:93], v[50:65]
	s_waitcnt lgkmcnt(0)
	v_mfma_f32_32x32x16_bf16 v[50:65], v[216:219], v[94:97], v[50:65]
	v_mfma_f32_32x32x16_bf16 v[34:49], v[212:215], v[122:125], v[34:49]
	s_nop 10
	v_mul_f32_e64 v50, v50, s12
	v_mul_f32_e64 v51, v51, s12
	v_mul_f32_e64 v54, v54, s12
	v_mul_f32_e64 v55, v55, s12
	v_exp_f32_e32 v50, v50
	v_exp_f32_e32 v51, v51
	v_pk_mul_f32 v[52:53], v[52:53], s[12:13] op_sel_hi:[1,0]
	v_exp_f32_e32 v54, v54
	v_exp_f32_e32 v55, v55
	v_mfma_f32_32x32x16_bf16 v[34:49], v[216:219], v[126:129], v[34:49]
	v_add_f32_e64 v50, v50, 1.0
	v_add_f32_e64 v51, v51, 1.0
	v_exp_f32_e32 v52, v52
	v_rcp_f32_e32 v50, v50
	v_rcp_f32_e32 v51, v51
	v_exp_f32_e32 v53, v53
	v_pk_add_f32 v[54:55], v[54:55], 1.0 op_sel_hi:[1,0]
	ds_read2st64_b32 v[212:213], v175 offset0:68 offset1:70
	s_nop 3
	v_pk_mul_f32 v[34:35], v[34:35], s[12:13] op_sel_hi:[1,0]
	v_pk_add_f32 v[52:53], v[52:53], 1.0 op_sel_hi:[1,0]
	v_exp_f32_e32 v214, v34
	v_exp_f32_e32 v215, v35
	v_pk_mul_f32 v[34:35], v[182:183], v[50:51]
	v_rcp_f32_e32 v54, v54
	v_exp_f32_e32 v34, v34
	v_exp_f32_e32 v35, v35
	v_pk_add_f32 v[50:51], v[214:215], 1.0 op_sel_hi:[1,0]
	v_rcp_f32_e32 v55, v55
	v_rcp_f32_e32 v50, v50
	v_pk_fma_f32 v[214:215], v[34:35], v[34:35], 1.0 op_sel_hi:[1,1,0] neg_lo:[1,0,0] neg_hi:[1,0,0]
	v_rcp_f32_e32 v51, v51
	v_sqrt_f32_e32 v214, v214
	v_sqrt_f32_e32 v215, v215
	v_rcp_f32_e32 v52, v52
	v_rcp_f32_e32 v53, v53
	v_pk_mul_f32 v[38:39], v[38:39], s[12:13] op_sel_hi:[1,0]
	v_pk_mul_f32 v[50:51], v[50:51], v[214:215]
	v_pk_mul_f32 v[36:37], v[36:37], s[12:13] op_sel_hi:[1,0]
	v_exp_f32_e32 v216, v38
	v_exp_f32_e32 v217, v39
	v_pk_mul_f32 v[38:39], v[182:183], v[54:55]
	s_waitcnt lgkmcnt(0)
	v_pk_mul_f32 v[50:51], v[212:213], v[50:51]
	v_exp_f32_e32 v212, v36
	v_exp_f32_e32 v213, v37
	v_pk_mul_f32 v[36:37], v[182:183], v[52:53]
	v_exp_f32_e32 v38, v38
	v_exp_f32_e32 v39, v39
	v_exp_f32_e32 v36, v36
	v_exp_f32_e32 v37, v37
	v_pk_add_f32 v[54:55], v[216:217], 1.0 op_sel_hi:[1,0]
	v_pk_add_f32 v[52:53], v[212:213], 1.0 op_sel_hi:[1,0]
	v_rcp_f32_e32 v216, v54
	v_rcp_f32_e32 v217, v55
	v_pk_fma_f32 v[54:55], v[38:39], v[38:39], 1.0 op_sel_hi:[1,1,0] neg_lo:[1,0,0] neg_hi:[1,0,0]
	v_pk_fma_f32 v[212:213], v[36:37], v[36:37], 1.0 op_sel_hi:[1,1,0] neg_lo:[1,0,0] neg_hi:[1,0,0]
	v_sqrt_f32_e32 v218, v54
	v_sqrt_f32_e32 v219, v55
	v_pk_mul_f32 v[54:55], v[56:57], s[12:13] op_sel_hi:[1,0]
	v_rcp_f32_e32 v52, v52
	v_rcp_f32_e32 v53, v53
	v_sqrt_f32_e32 v212, v212
	v_sqrt_f32_e32 v213, v213
	v_exp_f32_e32 v56, v54
	v_exp_f32_e32 v57, v55
	ds_read2st64_b32 v[214:215], v175 offset0:72 offset1:74
	v_pk_mul_f32 v[58:59], v[58:59], s[12:13] op_sel_hi:[1,0]
	v_pk_mul_f32 v[52:53], v[52:53], v[212:213]
	ds_read2st64_b32 v[212:213], v175 offset0:84 offset1:86
	v_pk_add_f32 v[56:57], v[56:57], 1.0 op_sel_hi:[1,0]
	v_exp_f32_e32 v58, v58
	v_exp_f32_e32 v59, v59
	v_rcp_f32_e32 v56, v56
	v_rcp_f32_e32 v57, v57
	s_waitcnt lgkmcnt(1)
; template <bool FINAL, int z> __device__ __forceinline__ void rglru_blocks(LAS unsigned char* XCB, LAS float* XCF, LAS float* HS, const bf16x8 (&wa)[8], const bf16x8 (&wx)[8],
;         float ba, float bxx, float sp8, int r, int hh, int chl, float& st, float& CA, float& CB) {
;     ...
;             for (int i = 0; i < 16; i += 2) {
;                 typedef float f2 __attribute__((ext_vector_type(2)));
;                 const f2 xc = {XCF[(32 * tb + crow(i, hh)) * 128 + chl], XCF[(32 * tb + crow(i + 1, hh)) * 128 + chl]};
;                 const f2 ta = (f2){ya[i], ya[i + 1]} * -1.4426950408889634f, tx = (f2){yx[i], yx[i + 1]} * -1.4426950408889634f;
;                 f2 ea, ex; ea.x = __builtin_amdgcn_exp2f(ta.x); ea.y = __builtin_amdgcn_exp2f(ta.y); ex.x = __builtin_amdgcn_exp2f(tx.x); ex.y = __builtin_amdgcn_exp2f(tx.y);
;                 const f2 da = ea + 1.0f, dx = ex + 1.0f;
;                 f2 rg, ig; rg.x = __builtin_amdgcn_rcpf(da.x); rg.y = __builtin_amdgcn_rcpf(da.y); ig.x = __builtin_amdgcn_rcpf(dx.x); ig.y = __builtin_amdgcn_rcpf(dx.y);
;                 const f2 la = rg * sp8; f2 a; a.x = __builtin_amdgcn_exp2f(la.x); a.y = __builtin_amdgcn_exp2f(la.y);
;                 const f2 om = a * -a + 1.0f; f2 sq; sq.x = __builtin_amdgcn_sqrtf(om.x); sq.y = __builtin_amdgcn_sqrtf(om.y);
;                 const f2 b = sq * ig * xc;
;                 av[i] = a.x; av[i + 1] = a.y; bv[i] = b.x; bv[i + 1] = b.y; }
;             float Ag[4], Bg[4], Ap[4], Bp[4];
; #pragma unroll
;             for (int g = 0; g < 4; ++g) { float A = 1.f, B = 0.f;
; #pragma unroll
;                 for (int k = 0; k < 4; ++k) { const int kk = z ? 3 - k : k; B = B * av[4 * g + kk] + bv[4 * g + kk]; A *= av[4 * g + kk]; }
;                 Ag[g] = A; Bg[g] = B; Ap[g] = __shfl_xor(A, 32); Bp[g] = __shfl_xor(B, 32); }
;             float ent[4]; float cur = st;
; #pragma unroll
;             for (int gi = 0; gi < 4; ++gi) { const int g = z ? 3 - gi : gi;
;                 const bool own_first = z ? (hh == 1) : (hh == 0);
;                 if (own_first) { ent[g] = cur; cur = Ag[g] * cur + Bg[g]; CB = Ag[g] * CB + Bg[g]; CA *= Ag[g]; cur = Ap[g] * cur + Bp[g]; CB = Ap[g] * CB + Bp[g]; CA *= Ap[g]; }
;                 else { cur = Ap[g] * cur + Bp[g]; CB = Ap[g] * CB + Bp[g]; CA *= Ap[g]; ent[g] = cur; cur = Ag[g] * cur + Bg[g]; CB = Ag[g] * CB + Bg[g]; CA *= Ag[g]; } }
	v_pk_mul_f32 v[54:55], v[214:215], v[52:53]
	v_pk_mul_f32 v[52:53], v[216:217], v[218:219]
	v_pk_mul_f32 v[40:41], v[40:41], s[12:13] op_sel_hi:[1,0]
	v_pk_add_f32 v[58:59], v[58:59], 1.0 op_sel_hi:[1,0]
	s_waitcnt lgkmcnt(0)
	v_pk_mul_f32 v[52:53], v[212:213], v[52:53]
	v_exp_f32_e32 v212, v40
	v_exp_f32_e32 v213, v41
	v_pk_mul_f32 v[40:41], v[182:183], v[56:57]
	v_rcp_f32_e32 v58, v58
	v_rcp_f32_e32 v59, v59
	v_pk_mul_f32 v[60:61], v[60:61], s[12:13] op_sel_hi:[1,0]
	v_exp_f32_e32 v40, v40
	v_exp_f32_e32 v41, v41
	v_exp_f32_e32 v60, v60
	v_exp_f32_e32 v61, v61
	v_pk_mul_f32 v[64:65], v[64:65], s[12:13] op_sel_hi:[1,0]
	v_pk_mul_f32 v[42:43], v[42:43], s[12:13] op_sel_hi:[1,0]
	v_exp_f32_e32 v64, v64
	v_exp_f32_e32 v65, v65
	v_exp_f32_e32 v216, v42
	v_exp_f32_e32 v217, v43
	v_pk_mul_f32 v[42:43], v[182:183], v[58:59]
	v_pk_mul_f32 v[62:63], v[62:63], s[12:13] op_sel_hi:[1,0]
	v_pk_add_f32 v[56:57], v[212:213], 1.0 op_sel_hi:[1,0]
	v_pk_fma_f32 v[212:213], v[40:41], v[40:41], 1.0 op_sel_hi:[1,1,0] neg_lo:[1,0,0] neg_hi:[1,0,0]
	v_exp_f32_e32 v42, v42
	v_exp_f32_e32 v43, v43
	v_pk_add_f32 v[60:61], v[60:61], 1.0 op_sel_hi:[1,0]
	v_exp_f32_e32 v62, v62
	v_exp_f32_e32 v63, v63
	v_rcp_f32_e32 v56, v56
	v_rcp_f32_e32 v57, v57
	v_sqrt_f32_e32 v212, v212
	v_sqrt_f32_e32 v213, v213
	v_rcp_f32_e32 v60, v60
	v_rcp_f32_e32 v61, v61
	v_pk_add_f32 v[64:65], v[64:65], 1.0 op_sel_hi:[1,0]
	v_pk_add_f32 v[58:59], v[216:217], 1.0 op_sel_hi:[1,0]
	v_rcp_f32_e32 v64, v64
	v_rcp_f32_e32 v65, v65
	v_pk_fma_f32 v[216:217], v[42:43], v[42:43], 1.0 op_sel_hi:[1,1,0] neg_lo:[1,0,0] neg_hi:[1,0,0]
	v_pk_add_f32 v[62:63], v[62:63], 1.0 op_sel_hi:[1,0]
	v_pk_mul_f32 v[56:57], v[56:57], v[212:213]
	ds_read2st64_b32 v[212:213], v175 offset0:100 offset1:102
	v_rcp_f32_e32 v58, v58
	v_rcp_f32_e32 v59, v59
	v_sqrt_f32_e32 v216, v216
	v_sqrt_f32_e32 v217, v217
	v_pk_mul_f32 v[44:45], v[44:45], s[12:13] op_sel_hi:[1,0]
	v_pk_mul_f32 v[60:61], v[182:183], v[60:61]
	v_rcp_f32_e32 v62, v62
	v_rcp_f32_e32 v63, v63
	v_exp_f32_e32 v44, v44
	v_exp_f32_e32 v45, v45
	v_exp_f32_e32 v60, v60
	v_exp_f32_e32 v61, v61
	v_pk_mul_f32 v[48:49], v[48:49], s[12:13] op_sel_hi:[1,0]
	v_pk_mul_f32 v[64:65], v[182:183], v[64:65]
	v_exp_f32_e32 v48, v48
	v_exp_f32_e32 v49, v49
	v_exp_f32_e32 v64, v64
	v_exp_f32_e32 v65, v65
	v_pk_mul_f32 v[58:59], v[58:59], v[216:217]
	v_pk_mul_f32 v[46:47], v[46:47], s[12:13] op_sel_hi:[1,0]
	v_pk_mul_f32 v[62:63], v[182:183], v[62:63]
	s_waitcnt lgkmcnt(0)
	v_pk_mul_f32 v[58:59], v[212:213], v[58:59]
	v_pk_add_f32 v[44:45], v[44:45], 1.0 op_sel_hi:[1,0]
	v_pk_fma_f32 v[212:213], v[60:61], v[60:61], 1.0 op_sel_hi:[1,1,0] neg_lo:[1,0,0] neg_hi:[1,0,0]
	v_exp_f32_e32 v46, v46
	v_exp_f32_e32 v47, v47
	v_exp_f32_e32 v62, v62
	v_exp_f32_e32 v63, v63
	v_rcp_f32_e32 v44, v44
	v_rcp_f32_e32 v45, v45
	v_sqrt_f32_e32 v212, v212
	v_sqrt_f32_e32 v213, v213
	ds_read2st64_b32 v[214:215], v175 offset0:88 offset1:90
	v_pk_add_f32 v[48:49], v[48:49], 1.0 op_sel_hi:[1,0]
	v_pk_fma_f32 v[220:221], v[64:65], v[64:65], 1.0 op_sel_hi:[1,1,0] neg_lo:[1,0,0] neg_hi:[1,0,0]
	ds_read2st64_b32 v[218:219], v175 offset0:120 offset1:122
	v_rcp_f32_e32 v48, v48
	v_rcp_f32_e32 v49, v49
	v_sqrt_f32_e32 v220, v220
	v_sqrt_f32_e32 v221, v221
	v_pk_add_f32 v[46:47], v[46:47], 1.0 op_sel_hi:[1,0]
	v_pk_fma_f32 v[216:217], v[62:63], v[62:63], 1.0 op_sel_hi:[1,1,0] neg_lo:[1,0,0] neg_hi:[1,0,0]
	v_pk_mul_f32 v[44:45], v[44:45], v[212:213]
	ds_read2st64_b32 v[212:213], v175 offset0:116 offset1:118
	v_rcp_f32_e32 v46, v46
	v_rcp_f32_e32 v47, v47
	v_sqrt_f32_e32 v216, v216
	v_sqrt_f32_e32 v217, v217
	s_waitcnt lgkmcnt(2)
	v_pk_mul_f32 v[56:57], v[214:215], v[56:57]
	ds_read2st64_b32 v[214:215], v175 offset0:104 offset1:106
	v_pk_mul_f32 v[48:49], v[48:49], v[220:221]
	v_pk_mul_f32 v[46:47], v[46:47], v[216:217]
	s_waitcnt lgkmcnt(2)
	v_pk_mul_f32 v[48:49], v[218:219], v[48:49]
	s_waitcnt lgkmcnt(1)
	v_pk_mul_f32 v[46:47], v[212:213], v[46:47]
	v_fma_f32 v220, 0, v65, v49
	v_fma_f32 v220, v64, v220, v48
	v_mul_f32_e32 v221, v65, v64
	v_fma_f32 v220, v63, v220, v47
	v_mul_f32_e32 v221, v63, v221
	s_waitcnt lgkmcnt(0)
	v_pk_mul_f32 v[44:45], v[214:215], v[44:45]
	v_fma_f32 v220, v62, v220, v46
	v_mul_f32_e32 v221, v62, v221
	v_fma_f32 v218, 0, v61, v45
	ds_bpermute_b32 v222, v159, v221
	ds_bpermute_b32 v223, v159, v220
	v_fma_f32 v218, v60, v218, v44
	v_mul_f32_e32 v219, v61, v60
	v_fma_f32 v218, v43, v218, v59
	v_mul_f32_e32 v219, v43, v219
	v_fma_f32 v218, v42, v218, v58
	v_mul_f32_e32 v219, v42, v219
	v_fma_f32 v214, 0, v41, v57
	ds_bpermute_b32 v224, v159, v219
	ds_bpermute_b32 v225, v159, v218
	v_fma_f32 v226, v211, v221, v220
	v_fma_f32 v214, v40, v214, v56
	v_mul_f32_e32 v215, v41, v40
	s_waitcnt lgkmcnt(2)
	v_fma_f32 v226, v226, v222, v223
	v_fmac_f32_e32 v223, v211, v222
	v_fma_f32 v214, v39, v214, v53
	v_mul_f32_e32 v215, v39, v215
	v_fmac_f32_e32 v220, v221, v223
	v_fma_f32 v212, 0, v37, v55
	v_fma_f32 v214, v38, v214, v52
	v_mul_f32_e32 v215, v38, v215
	v_cndmask_b32_e64 v211, v220, v226, s[0:1]
	v_fma_f32 v212, v36, v212, v54
	v_mul_f32_e32 v213, v37, v36
	ds_bpermute_b32 v216, v159, v215
	ds_bpermute_b32 v217, v159, v214
	v_fma_f32 v220, v219, v211, v218
	v_fma_f32 v212, v35, v212, v51
	v_mul_f32_e32 v213, v35, v213
	s_waitcnt lgkmcnt(2)
	v_fma_f32 v220, v220, v224, v225
	v_fmac_f32_e32 v225, v211, v224
	v_fma_f32 v212, v34, v212, v50
	v_mul_f32_e32 v213, v34, v213
	v_fmac_f32_e32 v218, v219, v225
	ds_bpermute_b32 v213, v159, v213
	ds_bpermute_b32 v212, v159, v212
	v_cndmask_b32_e64 v218, v218, v220, s[0:1]
	v_fma_f32 v219, v215, v218, v214
	s_waitcnt lgkmcnt(2)
	v_fma_f32 v219, v219, v216, v217
	v_fmac_f32_e32 v217, v218, v216
	v_fmac_f32_e32 v214, v215, v217
	v_cndmask_b32_e64 v214, v214, v219, s[0:1]
	s_waitcnt lgkmcnt(0)
	v_fmac_f32_e32 v212, v214, v213
	v_cndmask_b32_e64 v212, v212, v219, s[0:1]
	v_fma_f32 v37, v37, v212, v55
	v_fmac_f32_e32 v54, v36, v37
	v_cndmask_b32_e64 v215, v217, v220, s[0:1]
	v_fma_f32 v35, v35, v54, v51
	v_fmac_f32_e32 v50, v34, v35
	v_fma_f32 v34, v41, v215, v57
	v_fmac_f32_e32 v56, v40, v34
	ds_write2st64_b32 v177, v56, v34 offset0:148 offset1:150
	v_fma_f32 v34, v39, v56, v53
	v_cndmask_b32_e64 v211, v225, v226, s[0:1]
	v_fmac_f32_e32 v52, v38, v34
	ds_write2st64_b32 v177, v52, v34 offset0:144 offset1:146
	v_fma_f32 v34, v61, v211, v45
	v_fmac_f32_e32 v44, v60, v34
	ds_write2st64_b32 v177, v44, v34 offset0:164 offset1:166
	v_fma_f32 v34, v43, v44, v59
	v_cndmask_b32_e64 v210, v223, v210, s[0:1]
	v_fmac_f32_e32 v58, v42, v34
	ds_write2st64_b32 v177, v58, v34 offset0:160 offset1:162
	v_fma_f32 v34, v65, v210, v49
	v_fmac_f32_e32 v48, v64, v34
	ds_write2st64_b32 v177, v48, v34 offset0:180 offset1:182
	v_fma_f32 v34, v63, v48, v47
	v_fmac_f32_e32 v46, v62, v34
	ds_write2st64_b32 v177, v54, v37 offset0:132 offset1:134
	ds_write2st64_b32 v177, v50, v35 offset0:128 offset1:130
	ds_write2st64_b32 v177, v46, v34 offset0:176 offset1:178
